# expert GEMM epilogues (SwiGLU and down): flat_store replaced by global_store so the stores no longer hold lgkmcnt ahead of the next unit's LDS waits
# speedup vs baseline: 1.0035x; 1.0035x over previous
.LBB0_783:
	s_mov_b32 s98, 0xc01d265f
	s_mov_b32 s100, 0xc0c00000
	v_mov_b32_e32 v203, 0x41000000
	s_add_i32 s2, 0, 0x20000
	s_nop 15
	s_nop 15
	v_add_u32_e32 v2, s2, v178
	ds_read_b128 v[10:13], v2
	v_readlane_b32 s3, v238, 9
	v_add_u32_e32 v18, s47, v175
	v_ashrrev_i32_e32 v19, 31, v18
	v_add_u32_e32 v6, s3, v179
	ds_read_b128 v[6:9], v6
	s_waitcnt lgkmcnt(0)
	v_pk_add_f32 v[24:25], v[158:159], v[10:11]
	v_pk_add_f32 v[22:23], v[160:161], v[12:13]
	v_min_f32_e32 v25, 0x40e00000, v25
	v_min_f32_e32 v24, 0x40e00000, v24
	v_pk_mul_f32 v[30:31], s[98:99], v[24:25] op_sel_hi:[0,1]
	v_min_f32_e32 v23, 0x40e00000, v23
	v_min_f32_e32 v22, 0x40e00000, v22
	v_exp_f32_e32 v30, v30
	v_exp_f32_e32 v31, v31
	v_add_u32_e32 v2, s3, v178
	v_pk_mul_f32 v[32:33], s[98:99], v[22:23] op_sel_hi:[0,1]
	ds_read_b128 v[14:17], v2
	v_exp_f32_e32 v32, v32
	v_exp_f32_e32 v33, v33
	v_pk_add_f32 v[30:31], v[30:31], 1.0 op_sel_hi:[1,0]
	v_add_u32_e32 v2, s2, v179
	v_rcp_f32_e32 v30, v30
	v_rcp_f32_e32 v31, v31
	v_pk_add_f32 v[32:33], v[32:33], 1.0 op_sel_hi:[1,0]
	s_waitcnt lgkmcnt(0)
	v_pk_add_f32 v[14:15], v[14:15], 1.0 op_sel_hi:[1,0]
	v_pk_add_f32 v[16:17], v[16:17], 1.0 op_sel_hi:[1,0]
	v_pk_add_f32 v[28:29], v[154:155], v[14:15]
	v_rcp_f32_e32 v32, v32
	v_rcp_f32_e32 v33, v33
	ds_read_b128 v[2:5], v2
	v_med3_f32 v28, v28, s100, v203
	v_pk_add_f32 v[26:27], v[156:157], v[16:17]
	v_med3_f32 v29, v29, s100, v203
	v_pk_mul_f32 v[24:25], v[24:25], v[30:31]
	v_med3_f32 v26, v26, s100, v203
	v_med3_f32 v27, v27, s100, v203
	v_pk_mul_f32 v[22:23], v[22:23], v[32:33]
	v_pk_mul_f32 v[154:155], v[28:29], v[24:25]
	v_pk_mul_f32 v[156:157], v[26:27], v[22:23]
	s_waitcnt lgkmcnt(0)
	v_pk_add_f32 v[22:23], v[152:153], v[4:5]
	v_pk_add_f32 v[24:25], v[150:151], v[2:3]
	v_min_f32_e32 v23, 0x40e00000, v23
	v_min_f32_e32 v22, 0x40e00000, v22
	v_min_f32_e32 v25, 0x40e00000, v25
	v_min_f32_e32 v24, 0x40e00000, v24
	v_pk_mul_f32 v[30:31], s[98:99], v[24:25] op_sel_hi:[0,1]
	v_pk_mul_f32 v[32:33], s[98:99], v[22:23] op_sel_hi:[0,1]
	v_exp_f32_e32 v30, v30
	v_exp_f32_e32 v31, v31
	v_exp_f32_e32 v32, v32
	v_exp_f32_e32 v33, v33
	v_pk_add_f32 v[6:7], v[6:7], 1.0 op_sel_hi:[1,0]
	v_pk_add_f32 v[8:9], v[8:9], 1.0 op_sel_hi:[1,0]
	v_pk_add_f32 v[26:27], v[148:149], v[8:9]
	v_pk_add_f32 v[30:31], v[30:31], 1.0 op_sel_hi:[1,0]
	v_pk_add_f32 v[28:29], v[146:147], v[6:7]
	v_pk_add_f32 v[32:33], v[32:33], 1.0 op_sel_hi:[1,0]
	v_rcp_f32_e32 v30, v30
	v_rcp_f32_e32 v31, v31
	v_rcp_f32_e32 v32, v32
	v_rcp_f32_e32 v33, v33
	v_med3_f32 v26, v26, s100, v203
	v_med3_f32 v28, v28, s100, v203
	v_med3_f32 v27, v27, s100, v203
	v_med3_f32 v29, v29, s100, v203
	v_pk_mul_f32 v[22:23], v[22:23], v[32:33]
	v_pk_mul_f32 v[24:25], v[24:25], v[30:31]
	v_pk_mul_f32 v[24:25], v[28:29], v[24:25]
	v_pk_mul_f32 v[26:27], v[26:27], v[22:23]
	v_cvt_pk_fp8_f32 v22, v154, v155
	v_cvt_pk_fp8_f32 v23, v24, v25
	v_add_u32_e32 v20, s48, v180
	v_lshlrev_b64 v[18:19], 10, v[18:19]
	v_cvt_pk_fp8_f32 v22, v156, v157 op_sel:[0,0,1]
	v_cvt_pk_fp8_f32 v23, v26, v27 op_sel:[0,0,1]
	v_ashrrev_i32_e32 v21, 31, v20
	v_lshl_add_u64 v[18:19], s[6:7], 0, v[18:19]
	v_lshl_add_u64 v[18:19], v[18:19], 0, v[20:21]
	global_store_dwordx2 v[18:19], v[22:23], off
	v_pk_add_f32 v[22:23], v[142:143], v[10:11]
	v_pk_add_f32 v[20:21], v[144:145], v[12:13]
	v_min_f32_e32 v23, 0x40e00000, v23
	v_min_f32_e32 v22, 0x40e00000, v22
	v_pk_mul_f32 v[28:29], s[98:99], v[22:23] op_sel_hi:[0,1]
	v_min_f32_e32 v21, 0x40e00000, v21
	v_min_f32_e32 v20, 0x40e00000, v20
	v_exp_f32_e32 v28, v28
	v_exp_f32_e32 v29, v29
	v_pk_mul_f32 v[30:31], s[98:99], v[20:21] op_sel_hi:[0,1]
	v_exp_f32_e32 v30, v30
	v_exp_f32_e32 v31, v31
	v_pk_add_f32 v[28:29], v[28:29], 1.0 op_sel_hi:[1,0]
	v_pk_add_f32 v[26:27], v[138:139], v[14:15]
	v_rcp_f32_e32 v28, v28
	v_rcp_f32_e32 v29, v29
	v_pk_add_f32 v[30:31], v[30:31], 1.0 op_sel_hi:[1,0]
	v_med3_f32 v26, v26, s100, v203
	v_rcp_f32_e32 v30, v30
	v_rcp_f32_e32 v31, v31
	v_pk_add_f32 v[24:25], v[140:141], v[16:17]
	v_med3_f32 v27, v27, s100, v203
	v_pk_mul_f32 v[22:23], v[22:23], v[28:29]
	v_med3_f32 v24, v24, s100, v203
	v_med3_f32 v25, v25, s100, v203
	v_pk_mul_f32 v[20:21], v[20:21], v[30:31]
	v_pk_mul_f32 v[32:33], v[26:27], v[22:23]
	v_pk_mul_f32 v[138:139], v[24:25], v[20:21]
	v_pk_add_f32 v[20:21], v[136:137], v[4:5]
	v_pk_add_f32 v[22:23], v[134:135], v[2:3]
	v_min_f32_e32 v21, 0x40e00000, v21
	v_min_f32_e32 v20, 0x40e00000, v20
	v_min_f32_e32 v23, 0x40e00000, v23
	v_min_f32_e32 v22, 0x40e00000, v22
	v_pk_mul_f32 v[28:29], s[98:99], v[22:23] op_sel_hi:[0,1]
	v_pk_mul_f32 v[30:31], s[98:99], v[20:21] op_sel_hi:[0,1]
	v_exp_f32_e32 v28, v28
	v_exp_f32_e32 v29, v29
	v_exp_f32_e32 v30, v30
	v_exp_f32_e32 v31, v31
	v_pk_add_f32 v[24:25], v[132:133], v[8:9]
	v_pk_add_f32 v[28:29], v[28:29], 1.0 op_sel_hi:[1,0]
	v_pk_add_f32 v[26:27], v[130:131], v[6:7]
	v_pk_add_f32 v[30:31], v[30:31], 1.0 op_sel_hi:[1,0]
	v_rcp_f32_e32 v28, v28
	v_rcp_f32_e32 v29, v29
	v_rcp_f32_e32 v30, v30
	v_rcp_f32_e32 v31, v31
	v_med3_f32 v24, v24, s100, v203
	v_med3_f32 v26, v26, s100, v203
	v_med3_f32 v25, v25, s100, v203
	v_med3_f32 v27, v27, s100, v203
	v_pk_mul_f32 v[20:21], v[20:21], v[30:31]
	v_pk_mul_f32 v[22:23], v[22:23], v[28:29]
	v_pk_mul_f32 v[22:23], v[26:27], v[22:23]
	v_pk_mul_f32 v[24:25], v[24:25], v[20:21]
	v_cvt_pk_fp8_f32 v20, v32, v33
	v_cvt_pk_fp8_f32 v21, v22, v23
	v_add_co_u32_e32 v22, vcc, s69, v18
	v_cvt_pk_fp8_f32 v20, v138, v139 op_sel:[0,0,1]
	v_cvt_pk_fp8_f32 v21, v24, v25 op_sel:[0,0,1]
	v_addc_co_u32_e32 v23, vcc, 0, v19, vcc
	v_pk_add_f32 v[26:27], v[122:123], v[14:15]
	global_store_dwordx2 v[22:23], v[20:21], off
	v_pk_add_f32 v[22:23], v[126:127], v[10:11]
	v_pk_add_f32 v[20:21], v[128:129], v[12:13]
	v_min_f32_e32 v23, 0x40e00000, v23
	v_min_f32_e32 v22, 0x40e00000, v22
	v_pk_mul_f32 v[28:29], s[98:99], v[22:23] op_sel_hi:[0,1]
	v_min_f32_e32 v21, 0x40e00000, v21
	v_min_f32_e32 v20, 0x40e00000, v20
	v_exp_f32_e32 v28, v28
	v_exp_f32_e32 v29, v29
	v_pk_mul_f32 v[30:31], s[98:99], v[20:21] op_sel_hi:[0,1]
	v_exp_f32_e32 v30, v30
	v_exp_f32_e32 v31, v31
	v_pk_add_f32 v[28:29], v[28:29], 1.0 op_sel_hi:[1,0]
	v_med3_f32 v26, v26, s100, v203
	v_rcp_f32_e32 v28, v28
	v_rcp_f32_e32 v29, v29
	v_pk_add_f32 v[30:31], v[30:31], 1.0 op_sel_hi:[1,0]
	v_pk_add_f32 v[24:25], v[124:125], v[16:17]
	v_rcp_f32_e32 v30, v30
	v_rcp_f32_e32 v31, v31
	v_med3_f32 v27, v27, s100, v203
	v_pk_mul_f32 v[22:23], v[22:23], v[28:29]
	v_med3_f32 v24, v24, s100, v203
	v_med3_f32 v25, v25, s100, v203
	v_pk_mul_f32 v[20:21], v[20:21], v[30:31]
	v_pk_mul_f32 v[32:33], v[26:27], v[22:23]
	v_pk_mul_f32 v[122:123], v[24:25], v[20:21]
	v_pk_add_f32 v[20:21], v[120:121], v[4:5]
	v_pk_add_f32 v[22:23], v[118:119], v[2:3]
	v_min_f32_e32 v21, 0x40e00000, v21
	v_min_f32_e32 v20, 0x40e00000, v20
	v_min_f32_e32 v23, 0x40e00000, v23
	v_min_f32_e32 v22, 0x40e00000, v22
	v_pk_mul_f32 v[28:29], s[98:99], v[22:23] op_sel_hi:[0,1]
	v_pk_mul_f32 v[30:31], s[98:99], v[20:21] op_sel_hi:[0,1]
	v_exp_f32_e32 v28, v28
	v_exp_f32_e32 v29, v29
	v_exp_f32_e32 v30, v30
	v_exp_f32_e32 v31, v31
	v_pk_add_f32 v[24:25], v[116:117], v[8:9]
	v_pk_add_f32 v[28:29], v[28:29], 1.0 op_sel_hi:[1,0]
	v_pk_add_f32 v[26:27], v[114:115], v[6:7]
	v_pk_add_f32 v[30:31], v[30:31], 1.0 op_sel_hi:[1,0]
	v_rcp_f32_e32 v28, v28
	v_rcp_f32_e32 v29, v29
	v_rcp_f32_e32 v30, v30
	v_rcp_f32_e32 v31, v31
	v_med3_f32 v24, v24, s100, v203
	v_med3_f32 v26, v26, s100, v203
	v_med3_f32 v25, v25, s100, v203
	v_med3_f32 v27, v27, s100, v203
	v_pk_mul_f32 v[20:21], v[20:21], v[30:31]
	v_pk_mul_f32 v[22:23], v[22:23], v[28:29]
	v_pk_mul_f32 v[22:23], v[26:27], v[22:23]
	v_pk_mul_f32 v[24:25], v[24:25], v[20:21]
	v_cvt_pk_fp8_f32 v20, v32, v33
	v_cvt_pk_fp8_f32 v21, v22, v23
	v_add_co_u32_e32 v22, vcc, s67, v18
	v_cvt_pk_fp8_f32 v20, v122, v123 op_sel:[0,0,1]
	v_cvt_pk_fp8_f32 v21, v24, v25 op_sel:[0,0,1]
	v_addc_co_u32_e32 v23, vcc, 0, v19, vcc
	v_pk_add_f32 v[26:27], v[106:107], v[14:15]
	global_store_dwordx2 v[22:23], v[20:21], off
	v_pk_add_f32 v[22:23], v[110:111], v[10:11]
	v_pk_add_f32 v[20:21], v[112:113], v[12:13]
	v_min_f32_e32 v23, 0x40e00000, v23
	v_min_f32_e32 v22, 0x40e00000, v22
	v_pk_mul_f32 v[28:29], s[98:99], v[22:23] op_sel_hi:[0,1]
	v_min_f32_e32 v21, 0x40e00000, v21
	v_min_f32_e32 v20, 0x40e00000, v20
	v_exp_f32_e32 v28, v28
	v_exp_f32_e32 v29, v29
	v_pk_mul_f32 v[30:31], s[98:99], v[20:21] op_sel_hi:[0,1]
	v_exp_f32_e32 v30, v30
	v_exp_f32_e32 v31, v31
	v_pk_add_f32 v[28:29], v[28:29], 1.0 op_sel_hi:[1,0]
	v_med3_f32 v26, v26, s100, v203
	v_rcp_f32_e32 v28, v28
	v_rcp_f32_e32 v29, v29
	v_pk_add_f32 v[30:31], v[30:31], 1.0 op_sel_hi:[1,0]
	v_pk_add_f32 v[24:25], v[108:109], v[16:17]
	v_rcp_f32_e32 v30, v30
	v_rcp_f32_e32 v31, v31
	v_med3_f32 v27, v27, s100, v203
	v_pk_mul_f32 v[22:23], v[22:23], v[28:29]
	v_med3_f32 v24, v24, s100, v203
	v_med3_f32 v25, v25, s100, v203
	v_pk_mul_f32 v[20:21], v[20:21], v[30:31]
	v_pk_mul_f32 v[32:33], v[26:27], v[22:23]
	v_pk_mul_f32 v[106:107], v[24:25], v[20:21]
	v_pk_add_f32 v[20:21], v[104:105], v[4:5]
	v_pk_add_f32 v[22:23], v[102:103], v[2:3]
	v_min_f32_e32 v21, 0x40e00000, v21
	v_min_f32_e32 v20, 0x40e00000, v20
	v_min_f32_e32 v23, 0x40e00000, v23
	v_min_f32_e32 v22, 0x40e00000, v22
	v_pk_mul_f32 v[28:29], s[98:99], v[22:23] op_sel_hi:[0,1]
	v_pk_mul_f32 v[30:31], s[98:99], v[20:21] op_sel_hi:[0,1]
	v_exp_f32_e32 v28, v28
	v_exp_f32_e32 v29, v29
	v_exp_f32_e32 v30, v30
	v_exp_f32_e32 v31, v31
	v_pk_add_f32 v[24:25], v[100:101], v[8:9]
	v_pk_add_f32 v[28:29], v[28:29], 1.0 op_sel_hi:[1,0]
	v_pk_add_f32 v[26:27], v[98:99], v[6:7]
	v_pk_add_f32 v[30:31], v[30:31], 1.0 op_sel_hi:[1,0]
	v_rcp_f32_e32 v28, v28
	v_rcp_f32_e32 v29, v29
	v_rcp_f32_e32 v30, v30
	v_rcp_f32_e32 v31, v31
	v_med3_f32 v24, v24, s100, v203
	v_med3_f32 v26, v26, s100, v203
	v_med3_f32 v25, v25, s100, v203
	v_med3_f32 v27, v27, s100, v203
	v_pk_mul_f32 v[20:21], v[20:21], v[30:31]
	v_pk_mul_f32 v[22:23], v[22:23], v[28:29]
	v_pk_mul_f32 v[22:23], v[26:27], v[22:23]
	v_pk_mul_f32 v[24:25], v[24:25], v[20:21]
	v_cvt_pk_fp8_f32 v20, v32, v33
	v_cvt_pk_fp8_f32 v21, v22, v23
	s_mov_b32 s2, 0xc000
	v_add_co_u32_e32 v22, vcc, s2, v18
	v_cvt_pk_fp8_f32 v20, v106, v107 op_sel:[0,0,1]
	v_cvt_pk_fp8_f32 v21, v24, v25 op_sel:[0,0,1]
	v_addc_co_u32_e32 v23, vcc, 0, v19, vcc
	v_pk_add_f32 v[26:27], v[90:91], v[14:15]
	global_store_dwordx2 v[22:23], v[20:21], off
	v_pk_add_f32 v[22:23], v[94:95], v[10:11]
	v_pk_add_f32 v[20:21], v[96:97], v[12:13]
	v_min_f32_e32 v23, 0x40e00000, v23
	v_min_f32_e32 v22, 0x40e00000, v22
	v_pk_mul_f32 v[28:29], s[98:99], v[22:23] op_sel_hi:[0,1]
	v_min_f32_e32 v21, 0x40e00000, v21
	v_min_f32_e32 v20, 0x40e00000, v20
	v_exp_f32_e32 v28, v28
	v_exp_f32_e32 v29, v29
	v_pk_mul_f32 v[30:31], s[98:99], v[20:21] op_sel_hi:[0,1]
	v_exp_f32_e32 v30, v30
	v_exp_f32_e32 v31, v31
	v_pk_add_f32 v[28:29], v[28:29], 1.0 op_sel_hi:[1,0]
	v_med3_f32 v26, v26, s100, v203
	v_rcp_f32_e32 v28, v28
	v_rcp_f32_e32 v29, v29
	v_pk_add_f32 v[30:31], v[30:31], 1.0 op_sel_hi:[1,0]
	v_pk_add_f32 v[24:25], v[92:93], v[16:17]
	v_rcp_f32_e32 v30, v30
	v_rcp_f32_e32 v31, v31
	v_med3_f32 v27, v27, s100, v203
	v_pk_mul_f32 v[22:23], v[22:23], v[28:29]
	v_med3_f32 v24, v24, s100, v203
	v_med3_f32 v25, v25, s100, v203
	v_pk_mul_f32 v[20:21], v[20:21], v[30:31]
	v_pk_mul_f32 v[32:33], v[26:27], v[22:23]
	v_pk_mul_f32 v[90:91], v[24:25], v[20:21]
	v_pk_add_f32 v[20:21], v[88:89], v[4:5]
	v_pk_add_f32 v[22:23], v[86:87], v[2:3]
	v_min_f32_e32 v21, 0x40e00000, v21
	v_min_f32_e32 v20, 0x40e00000, v20
	v_min_f32_e32 v23, 0x40e00000, v23
	v_min_f32_e32 v22, 0x40e00000, v22
	v_pk_mul_f32 v[28:29], s[98:99], v[22:23] op_sel_hi:[0,1]
	v_pk_mul_f32 v[30:31], s[98:99], v[20:21] op_sel_hi:[0,1]
	v_exp_f32_e32 v28, v28
	v_exp_f32_e32 v29, v29
	v_exp_f32_e32 v30, v30
	v_exp_f32_e32 v31, v31
	v_pk_add_f32 v[24:25], v[84:85], v[8:9]
	v_pk_add_f32 v[28:29], v[28:29], 1.0 op_sel_hi:[1,0]
	v_pk_add_f32 v[26:27], v[82:83], v[6:7]
	v_pk_add_f32 v[30:31], v[30:31], 1.0 op_sel_hi:[1,0]
	v_rcp_f32_e32 v28, v28
	v_rcp_f32_e32 v29, v29
	v_rcp_f32_e32 v30, v30
	v_rcp_f32_e32 v31, v31
	v_med3_f32 v24, v24, s100, v203
	v_med3_f32 v26, v26, s100, v203
	v_med3_f32 v25, v25, s100, v203
	v_med3_f32 v27, v27, s100, v203
	v_pk_mul_f32 v[20:21], v[20:21], v[30:31]
	v_pk_mul_f32 v[22:23], v[22:23], v[28:29]
	v_pk_mul_f32 v[22:23], v[26:27], v[22:23]
	v_pk_mul_f32 v[24:25], v[24:25], v[20:21]
	v_cvt_pk_fp8_f32 v20, v32, v33
	v_cvt_pk_fp8_f32 v21, v22, v23
	s_mov_b32 s2, 0x20000
	v_add_co_u32_e32 v22, vcc, s2, v18
	v_cvt_pk_fp8_f32 v20, v90, v91 op_sel:[0,0,1]
	v_cvt_pk_fp8_f32 v21, v24, v25 op_sel:[0,0,1]
	v_addc_co_u32_e32 v23, vcc, 0, v19, vcc
	v_pk_add_f32 v[26:27], v[74:75], v[14:15]
	global_store_dwordx2 v[22:23], v[20:21], off
	v_pk_add_f32 v[22:23], v[78:79], v[10:11]
	v_pk_add_f32 v[20:21], v[80:81], v[12:13]
	v_min_f32_e32 v23, 0x40e00000, v23
	v_min_f32_e32 v22, 0x40e00000, v22
	v_pk_mul_f32 v[28:29], s[98:99], v[22:23] op_sel_hi:[0,1]
	v_min_f32_e32 v21, 0x40e00000, v21
	v_min_f32_e32 v20, 0x40e00000, v20
	v_exp_f32_e32 v28, v28
	v_exp_f32_e32 v29, v29
	v_pk_mul_f32 v[30:31], s[98:99], v[20:21] op_sel_hi:[0,1]
	v_exp_f32_e32 v30, v30
	v_exp_f32_e32 v31, v31
	v_pk_add_f32 v[28:29], v[28:29], 1.0 op_sel_hi:[1,0]
	v_med3_f32 v26, v26, s100, v203
	v_rcp_f32_e32 v28, v28
	v_rcp_f32_e32 v29, v29
	v_pk_add_f32 v[30:31], v[30:31], 1.0 op_sel_hi:[1,0]
	v_pk_add_f32 v[24:25], v[76:77], v[16:17]
	v_rcp_f32_e32 v30, v30
	v_rcp_f32_e32 v31, v31
	v_med3_f32 v27, v27, s100, v203
	v_pk_mul_f32 v[22:23], v[22:23], v[28:29]
	v_med3_f32 v24, v24, s100, v203
	v_med3_f32 v25, v25, s100, v203
	v_pk_mul_f32 v[20:21], v[20:21], v[30:31]
	v_pk_mul_f32 v[32:33], v[26:27], v[22:23]
	v_pk_mul_f32 v[74:75], v[24:25], v[20:21]
	v_pk_add_f32 v[20:21], v[72:73], v[4:5]
	v_pk_add_f32 v[22:23], v[70:71], v[2:3]
	v_min_f32_e32 v21, 0x40e00000, v21
	v_min_f32_e32 v20, 0x40e00000, v20
	v_min_f32_e32 v23, 0x40e00000, v23
	v_min_f32_e32 v22, 0x40e00000, v22
	v_pk_mul_f32 v[28:29], s[98:99], v[22:23] op_sel_hi:[0,1]
	v_pk_mul_f32 v[30:31], s[98:99], v[20:21] op_sel_hi:[0,1]
	v_exp_f32_e32 v28, v28
	v_exp_f32_e32 v29, v29
	v_exp_f32_e32 v30, v30
	v_exp_f32_e32 v31, v31
	v_pk_add_f32 v[24:25], v[68:69], v[8:9]
	v_pk_add_f32 v[28:29], v[28:29], 1.0 op_sel_hi:[1,0]
	v_pk_add_f32 v[26:27], v[66:67], v[6:7]
	v_pk_add_f32 v[30:31], v[30:31], 1.0 op_sel_hi:[1,0]
	v_rcp_f32_e32 v28, v28
	v_rcp_f32_e32 v29, v29
	v_rcp_f32_e32 v30, v30
	v_rcp_f32_e32 v31, v31
	v_med3_f32 v24, v24, s100, v203
	v_med3_f32 v26, v26, s100, v203
	v_med3_f32 v25, v25, s100, v203
	v_med3_f32 v27, v27, s100, v203
	v_pk_mul_f32 v[20:21], v[20:21], v[30:31]
	v_pk_mul_f32 v[22:23], v[22:23], v[28:29]
	v_pk_mul_f32 v[22:23], v[26:27], v[22:23]
	v_pk_mul_f32 v[24:25], v[24:25], v[20:21]
	v_cvt_pk_fp8_f32 v20, v32, v33
	v_cvt_pk_fp8_f32 v21, v22, v23
	s_mov_b32 s2, 0x24000
	v_add_co_u32_e32 v22, vcc, s2, v18
	v_cvt_pk_fp8_f32 v20, v74, v75 op_sel:[0,0,1]
	v_cvt_pk_fp8_f32 v21, v24, v25 op_sel:[0,0,1]
	v_addc_co_u32_e32 v23, vcc, 0, v19, vcc
	v_pk_add_f32 v[26:27], v[58:59], v[14:15]
	global_store_dwordx2 v[22:23], v[20:21], off
	v_pk_add_f32 v[22:23], v[62:63], v[10:11]
	v_pk_add_f32 v[20:21], v[64:65], v[12:13]
	v_min_f32_e32 v23, 0x40e00000, v23
	v_min_f32_e32 v22, 0x40e00000, v22
	v_pk_mul_f32 v[28:29], s[98:99], v[22:23] op_sel_hi:[0,1]
	v_min_f32_e32 v21, 0x40e00000, v21
	v_min_f32_e32 v20, 0x40e00000, v20
	v_exp_f32_e32 v28, v28
	v_exp_f32_e32 v29, v29
	v_pk_mul_f32 v[30:31], s[98:99], v[20:21] op_sel_hi:[0,1]
	v_exp_f32_e32 v30, v30
	v_exp_f32_e32 v31, v31
	v_pk_add_f32 v[28:29], v[28:29], 1.0 op_sel_hi:[1,0]
	v_med3_f32 v26, v26, s100, v203
	v_rcp_f32_e32 v28, v28
	v_rcp_f32_e32 v29, v29
	v_pk_add_f32 v[30:31], v[30:31], 1.0 op_sel_hi:[1,0]
	v_pk_add_f32 v[24:25], v[60:61], v[16:17]
	v_rcp_f32_e32 v30, v30
	v_rcp_f32_e32 v31, v31
	v_med3_f32 v27, v27, s100, v203
	v_pk_mul_f32 v[22:23], v[22:23], v[28:29]
	v_med3_f32 v24, v24, s100, v203
	v_med3_f32 v25, v25, s100, v203
	v_pk_mul_f32 v[20:21], v[20:21], v[30:31]
	v_pk_mul_f32 v[32:33], v[26:27], v[22:23]
	v_pk_mul_f32 v[58:59], v[24:25], v[20:21]
	v_pk_add_f32 v[20:21], v[56:57], v[4:5]
	v_pk_add_f32 v[22:23], v[54:55], v[2:3]
	v_min_f32_e32 v21, 0x40e00000, v21
	v_min_f32_e32 v20, 0x40e00000, v20
	v_min_f32_e32 v23, 0x40e00000, v23
	v_min_f32_e32 v22, 0x40e00000, v22
	v_pk_mul_f32 v[28:29], s[98:99], v[22:23] op_sel_hi:[0,1]
	v_pk_mul_f32 v[30:31], s[98:99], v[20:21] op_sel_hi:[0,1]
	v_exp_f32_e32 v28, v28
	v_exp_f32_e32 v29, v29
	v_exp_f32_e32 v30, v30
	v_exp_f32_e32 v31, v31
	v_pk_add_f32 v[24:25], v[52:53], v[8:9]
	v_pk_add_f32 v[28:29], v[28:29], 1.0 op_sel_hi:[1,0]
	v_pk_add_f32 v[26:27], v[50:51], v[6:7]
	v_pk_add_f32 v[30:31], v[30:31], 1.0 op_sel_hi:[1,0]
	v_rcp_f32_e32 v28, v28
	v_rcp_f32_e32 v29, v29
	v_rcp_f32_e32 v30, v30
	v_rcp_f32_e32 v31, v31
	v_med3_f32 v24, v24, s100, v203
	v_med3_f32 v26, v26, s100, v203
	v_med3_f32 v25, v25, s100, v203
	v_med3_f32 v27, v27, s100, v203
	v_pk_mul_f32 v[20:21], v[20:21], v[30:31]
	v_pk_mul_f32 v[22:23], v[22:23], v[28:29]
	v_pk_mul_f32 v[22:23], v[26:27], v[22:23]
	v_pk_mul_f32 v[24:25], v[24:25], v[20:21]
	v_cvt_pk_fp8_f32 v20, v32, v33
	v_cvt_pk_fp8_f32 v21, v22, v23
	s_mov_b32 s2, 0x28000
	v_add_co_u32_e32 v22, vcc, s2, v18
	v_cvt_pk_fp8_f32 v20, v58, v59 op_sel:[0,0,1]
	v_cvt_pk_fp8_f32 v21, v24, v25 op_sel:[0,0,1]
	v_pk_add_f32 v[10:11], v[46:47], v[10:11]
	v_addc_co_u32_e32 v23, vcc, 0, v19, vcc
	v_min_f32_e32 v11, 0x40e00000, v11
	v_min_f32_e32 v10, 0x40e00000, v10
	global_store_dwordx2 v[22:23], v[20:21], off
	v_pk_add_f32 v[12:13], v[48:49], v[12:13]
	v_pk_mul_f32 v[20:21], s[98:99], v[10:11] op_sel_hi:[0,1]
	v_min_f32_e32 v13, 0x40e00000, v13
	v_min_f32_e32 v12, 0x40e00000, v12
	v_exp_f32_e32 v20, v20
	v_exp_f32_e32 v21, v21
	v_pk_mul_f32 v[22:23], s[98:99], v[12:13] op_sel_hi:[0,1]
	v_exp_f32_e32 v22, v22
	v_exp_f32_e32 v23, v23
	v_pk_add_f32 v[20:21], v[20:21], 1.0 op_sel_hi:[1,0]
	v_pk_add_f32 v[14:15], v[42:43], v[14:15]
	v_rcp_f32_e32 v20, v20
	v_rcp_f32_e32 v21, v21
	v_pk_add_f32 v[22:23], v[22:23], 1.0 op_sel_hi:[1,0]
	v_med3_f32 v14, v14, s100, v203
	v_rcp_f32_e32 v22, v22
	v_rcp_f32_e32 v23, v23
	v_pk_add_f32 v[16:17], v[44:45], v[16:17]
	v_med3_f32 v15, v15, s100, v203
	v_pk_mul_f32 v[10:11], v[10:11], v[20:21]
	v_med3_f32 v16, v16, s100, v203
	v_med3_f32 v17, v17, s100, v203
	v_pk_mul_f32 v[12:13], v[12:13], v[22:23]
	v_pk_mul_f32 v[14:15], v[14:15], v[10:11]
	v_pk_add_f32 v[2:3], v[38:39], v[2:3]
	v_min_f32_e32 v3, 0x40e00000, v3
	v_min_f32_e32 v2, 0x40e00000, v2
	v_pk_mul_f32 v[16:17], v[16:17], v[12:13]
	v_pk_add_f32 v[4:5], v[40:41], v[4:5]
	v_pk_mul_f32 v[10:11], s[98:99], v[2:3] op_sel_hi:[0,1]
	v_min_f32_e32 v5, 0x40e00000, v5
	v_min_f32_e32 v4, 0x40e00000, v4
	v_exp_f32_e32 v10, v10
	v_exp_f32_e32 v11, v11
	v_pk_mul_f32 v[12:13], s[98:99], v[4:5] op_sel_hi:[0,1]
	v_exp_f32_e32 v12, v12
	v_exp_f32_e32 v13, v13
	v_pk_add_f32 v[10:11], v[10:11], 1.0 op_sel_hi:[1,0]
	v_pk_add_f32 v[6:7], v[34:35], v[6:7]
	v_rcp_f32_e32 v10, v10
	v_rcp_f32_e32 v11, v11
	v_pk_add_f32 v[12:13], v[12:13], 1.0 op_sel_hi:[1,0]
	v_med3_f32 v6, v6, s100, v203
	v_rcp_f32_e32 v12, v12
	v_rcp_f32_e32 v13, v13
	v_pk_add_f32 v[8:9], v[36:37], v[8:9]
	v_med3_f32 v7, v7, s100, v203
	v_pk_mul_f32 v[2:3], v[2:3], v[10:11]
	v_med3_f32 v8, v8, s100, v203
	v_med3_f32 v9, v9, s100, v203
	v_pk_mul_f32 v[4:5], v[4:5], v[12:13]
	v_pk_mul_f32 v[6:7], v[6:7], v[2:3]
	v_pk_mul_f32 v[4:5], v[8:9], v[4:5]
	v_cvt_pk_fp8_f32 v2, v14, v15
	v_cvt_pk_fp8_f32 v3, v6, v7
	s_mov_b64 s[2:3], -1
	v_cvt_pk_fp8_f32 v2, v16, v17 op_sel:[0,0,1]
	v_cvt_pk_fp8_f32 v3, v4, v5 op_sel:[0,0,1]
	v_add_co_u32_e32 v4, vcc, 0x2c000, v18
	s_nop 1
	v_addc_co_u32_e32 v5, vcc, 0, v19, vcc
	s_andn2_b64 vcc, exec, s[14:15]
	global_store_dwordx2 v[4:5], v[2:3], off
	s_cbranch_vccnz .LBB0_772
	s_andn2_b64 vcc, exec, s[4:5]
	s_cbranch_vccnz .LBB0_771
	s_barrier
	s_branch .LBB0_771

.LBB0_876:
	s_add_i32 s11, 0, 0x20400
	s_nop 15
	s_nop 15
	v_add_u32_e32 v18, s11, v182
	s_add_i32 s19, 0, 0x20800
	ds_read_b128 v[14:17], v203
	ds_read_b128 v[10:13], v203 offset:16
	ds_read_b128 v[6:9], v203 offset:512
	ds_read_b128 v[2:5], v203 offset:528
	v_add_u32_e32 v19, s19, v182
	v_add_u32_e32 v20, s11, v183
	v_add_u32_e32 v21, s19, v183
	v_add_u32_e32 v22, s11, v184
	v_add_u32_e32 v23, s19, v184
	ds_read_b32 v33, v18
	ds_read_b32 v32, v19
	ds_read_b32 v31, v20
	ds_read_b32 v30, v21
	ds_read_b32 v29, v22
	ds_read_b32 v28, v23
	v_add_u32_e32 v18, s11, v181
	v_add_u32_e32 v20, s19, v181
	ds_read2_b32 v[24:25], v18 offset0:128 offset1:144
	ds_read2_b32 v[26:27], v20 offset0:128 offset1:144
	ds_read2_b32 v[18:19], v18 offset0:160 offset1:176
	ds_read2_b32 v[22:23], v20 offset0:160 offset1:176
	v_add_u32_e32 v20, s18, v185
	v_add_u32_e32 v162, s54, v177
	v_ashrrev_i32_e32 v21, 31, v20
	v_cmp_gt_i32_e32 vcc, s39, v162
	s_and_saveexec_b64 s[18:19], vcc
	s_cbranch_execz .LBB0_878
	v_add_u32_e32 v163, 0, v181
	v_add_u32_e32 v164, 0x20800, v163
	v_add_u32_e32 v163, 0x20400, v163
	ds_read_b32 v166, v164
	ds_read_b32 v165, v163
	s_waitcnt lgkmcnt(0)
	v_pk_add_f32 v[154:155], v[154:155], v[10:11]
	v_pk_add_f32 v[158:159], v[158:159], v[14:15]
	v_mul_f32_e32 v166, 0x41800000, v166
	v_pk_mul_f32 v[154:155], v[154:155], v[166:167] op_sel_hi:[1,0]
	v_pk_mul_f32 v[158:159], v[158:159], v[166:167] op_sel_hi:[1,0]
	v_cvt_pk_fp8_f32 v205, v154, v155
	v_pk_add_f32 v[154:155], v[156:157], v[12:13]
	v_pk_mul_f32 v[154:155], v[154:155], v[166:167] op_sel_hi:[1,0]
	v_pk_add_f32 v[150:151], v[150:151], v[6:7]
	v_pk_add_f32 v[146:147], v[146:147], v[2:3]
	v_cvt_pk_fp8_f32 v204, v158, v159
	v_cvt_pk_fp8_f32 v205, v154, v155 op_sel:[0,0,1]
	v_pk_mul_f32 v[150:151], v[150:151], v[166:167] op_sel_hi:[1,0]
	v_pk_mul_f32 v[146:147], v[146:147], v[166:167] op_sel_hi:[1,0]
	v_cvt_pk_fp8_f32 v154, v150, v151
	v_cvt_pk_fp8_f32 v155, v146, v147
	v_pk_add_f32 v[160:161], v[160:161], v[16:17]
	v_pk_add_f32 v[152:153], v[152:153], v[8:9]
	v_pk_mul_f32 v[160:161], v[160:161], v[166:167] op_sel_hi:[1,0]
	v_pk_add_f32 v[146:147], v[148:149], v[4:5]
	v_mov_b32_e32 v164, v167
	v_cvt_pk_fp8_f32 v204, v160, v161 op_sel:[0,0,1]
	v_pk_mul_f32 v[152:153], v[152:153], v[166:167] op_sel_hi:[1,0]
	v_pk_mul_f32 v[146:147], v[146:147], v[166:167] op_sel_hi:[1,0]
	v_ashrrev_i64 v[164:165], 22, v[164:165]
	v_cvt_pk_fp8_f32 v154, v152, v153 op_sel:[0,0,1]
	v_cvt_pk_fp8_f32 v155, v146, v147 op_sel:[0,0,1]
	v_lshl_add_u64 v[146:147], s[2:3], 0, v[164:165]
	v_lshl_add_u64 v[146:147], v[146:147], 0, v[20:21]
	global_store_dwordx2 v[146:147], v[204:205], off
	global_store_dwordx2 v[146:147], v[154:155], off offset:128
.LBB0_878:
	s_or_b64 exec, exec, s[18:19]
	v_add_u32_e32 v146, s54, v199
	v_cmp_gt_i32_e32 vcc, s39, v146
	s_and_saveexec_b64 s[18:19], vcc
	s_cbranch_execz .LBB0_880
	s_waitcnt lgkmcnt(0)
	v_mul_f32_e32 v146, 0x41800000, v32
	v_pk_add_f32 v[138:139], v[138:139], v[10:11]
	v_pk_mul_f32 v[138:139], v[138:139], v[146:147] op_sel_hi:[1,0]
	v_pk_add_f32 v[142:143], v[142:143], v[14:15]
	v_cvt_pk_fp8_f32 v149, v138, v139
	v_pk_add_f32 v[138:139], v[140:141], v[12:13]
	v_pk_mul_f32 v[142:143], v[142:143], v[146:147] op_sel_hi:[1,0]
	v_pk_mul_f32 v[138:139], v[138:139], v[146:147] op_sel_hi:[1,0]
	v_pk_add_f32 v[134:135], v[134:135], v[6:7]
	v_pk_add_f32 v[130:131], v[130:131], v[2:3]
	v_cvt_pk_fp8_f32 v148, v142, v143
	v_cvt_pk_fp8_f32 v149, v138, v139 op_sel:[0,0,1]
	v_pk_mul_f32 v[134:135], v[134:135], v[146:147] op_sel_hi:[1,0]
	v_pk_mul_f32 v[130:131], v[130:131], v[146:147] op_sel_hi:[1,0]
	v_cvt_pk_fp8_f32 v138, v134, v135
	v_cvt_pk_fp8_f32 v139, v130, v131
	v_pk_add_f32 v[144:145], v[144:145], v[16:17]
	v_pk_add_f32 v[136:137], v[136:137], v[8:9]
	v_pk_mul_f32 v[144:145], v[144:145], v[146:147] op_sel_hi:[1,0]
	v_pk_add_f32 v[130:131], v[132:133], v[4:5]
	v_mov_b32_e32 v32, v167
	v_cvt_pk_fp8_f32 v148, v144, v145 op_sel:[0,0,1]
	v_pk_mul_f32 v[136:137], v[136:137], v[146:147] op_sel_hi:[1,0]
	v_pk_mul_f32 v[130:131], v[130:131], v[146:147] op_sel_hi:[1,0]
	v_ashrrev_i64 v[32:33], 22, v[32:33]
	v_cvt_pk_fp8_f32 v138, v136, v137 op_sel:[0,0,1]
	v_cvt_pk_fp8_f32 v139, v130, v131 op_sel:[0,0,1]
	v_lshl_add_u64 v[32:33], s[2:3], 0, v[32:33]
	v_lshl_add_u64 v[32:33], v[32:33], 0, v[20:21]
	global_store_dwordx2 v[32:33], v[148:149], off
	global_store_dwordx2 v[32:33], v[138:139], off offset:128
.LBB0_880:
	s_or_b64 exec, exec, s[18:19]
	s_waitcnt lgkmcnt(0)
	v_add_u32_e32 v32, s54, v200
	v_cmp_gt_i32_e32 vcc, s39, v32
	s_and_saveexec_b64 s[18:19], vcc
	s_cbranch_execz .LBB0_882
	v_mul_f32_e32 v32, 0x41800000, v30
	v_pk_add_f32 v[122:123], v[122:123], v[10:11]
	v_pk_mul_f32 v[122:123], v[122:123], v[32:33] op_sel_hi:[1,0]
	v_pk_add_f32 v[126:127], v[126:127], v[14:15]
	v_cvt_pk_fp8_f32 v131, v122, v123
	v_pk_add_f32 v[122:123], v[124:125], v[12:13]
	v_pk_mul_f32 v[126:127], v[126:127], v[32:33] op_sel_hi:[1,0]
	v_pk_mul_f32 v[122:123], v[122:123], v[32:33] op_sel_hi:[1,0]
	v_pk_add_f32 v[118:119], v[118:119], v[6:7]
	v_pk_add_f32 v[114:115], v[114:115], v[2:3]
	v_cvt_pk_fp8_f32 v130, v126, v127
	v_cvt_pk_fp8_f32 v131, v122, v123 op_sel:[0,0,1]
	v_pk_mul_f32 v[118:119], v[118:119], v[32:33] op_sel_hi:[1,0]
	v_pk_mul_f32 v[114:115], v[114:115], v[32:33] op_sel_hi:[1,0]
	v_cvt_pk_fp8_f32 v122, v118, v119
	v_cvt_pk_fp8_f32 v123, v114, v115
	v_pk_add_f32 v[128:129], v[128:129], v[16:17]
	v_pk_add_f32 v[120:121], v[120:121], v[8:9]
	v_pk_mul_f32 v[128:129], v[128:129], v[32:33] op_sel_hi:[1,0]
	v_pk_add_f32 v[114:115], v[116:117], v[4:5]
	v_mov_b32_e32 v30, v167
	v_cvt_pk_fp8_f32 v130, v128, v129 op_sel:[0,0,1]
	v_pk_mul_f32 v[120:121], v[120:121], v[32:33] op_sel_hi:[1,0]
	v_pk_mul_f32 v[32:33], v[114:115], v[32:33] op_sel_hi:[1,0]
	v_ashrrev_i64 v[30:31], 22, v[30:31]
	v_cvt_pk_fp8_f32 v122, v120, v121 op_sel:[0,0,1]
	v_cvt_pk_fp8_f32 v123, v32, v33 op_sel:[0,0,1]
	v_lshl_add_u64 v[30:31], s[2:3], 0, v[30:31]
	v_lshl_add_u64 v[30:31], v[30:31], 0, v[20:21]
	global_store_dwordx2 v[30:31], v[130:131], off
	global_store_dwordx2 v[30:31], v[122:123], off offset:128
.LBB0_882:
	s_or_b64 exec, exec, s[18:19]
	v_add_u32_e32 v30, s54, v201
	v_cmp_gt_i32_e32 vcc, s39, v30
	s_and_saveexec_b64 s[18:19], vcc
	s_cbranch_execz .LBB0_884
	v_mul_f32_e32 v30, 0x41800000, v28
	v_pk_add_f32 v[110:111], v[110:111], v[14:15]
	v_pk_add_f32 v[32:33], v[112:113], v[16:17]
	v_pk_mul_f32 v[110:111], v[110:111], v[30:31] op_sel_hi:[1,0]
	v_cvt_pk_fp8_f32 v112, v110, v111
	v_pk_add_f32 v[106:107], v[106:107], v[10:11]
	v_pk_mul_f32 v[32:33], v[32:33], v[30:31] op_sel_hi:[1,0]
	v_pk_mul_f32 v[106:107], v[106:107], v[30:31] op_sel_hi:[1,0]
	v_pk_add_f32 v[102:103], v[102:103], v[6:7]
	v_pk_add_f32 v[98:99], v[98:99], v[2:3]
	v_cvt_pk_fp8_f32 v113, v106, v107
	v_cvt_pk_fp8_f32 v112, v32, v33 op_sel:[0,0,1]
	v_pk_add_f32 v[32:33], v[104:105], v[8:9]
	v_pk_mul_f32 v[102:103], v[102:103], v[30:31] op_sel_hi:[1,0]
	v_pk_mul_f32 v[98:99], v[98:99], v[30:31] op_sel_hi:[1,0]
	v_cvt_pk_fp8_f32 v104, v102, v103
	v_cvt_pk_fp8_f32 v105, v98, v99
	v_pk_add_f32 v[106:107], v[108:109], v[12:13]
	v_pk_add_f32 v[98:99], v[100:101], v[4:5]
	v_pk_mul_f32 v[106:107], v[106:107], v[30:31] op_sel_hi:[1,0]
	v_mov_b32_e32 v28, v167
	v_cvt_pk_fp8_f32 v113, v106, v107 op_sel:[0,0,1]
	v_pk_mul_f32 v[32:33], v[32:33], v[30:31] op_sel_hi:[1,0]
	v_pk_mul_f32 v[30:31], v[98:99], v[30:31] op_sel_hi:[1,0]
	v_ashrrev_i64 v[28:29], 22, v[28:29]
	v_cvt_pk_fp8_f32 v104, v32, v33 op_sel:[0,0,1]
	v_cvt_pk_fp8_f32 v105, v30, v31 op_sel:[0,0,1]
	v_lshl_add_u64 v[28:29], s[2:3], 0, v[28:29]
	v_lshl_add_u64 v[28:29], v[28:29], 0, v[20:21]
	global_store_dwordx2 v[28:29], v[112:113], off
	global_store_dwordx2 v[28:29], v[104:105], off offset:128
.LBB0_884:
	s_or_b64 exec, exec, s[18:19]
	v_add_u32_e32 v28, 0x80, v162
	v_cmp_gt_i32_e32 vcc, s39, v28
	s_and_saveexec_b64 s[18:19], vcc
	s_cbranch_execz .LBB0_886
	v_mul_f32_e32 v26, 0x41800000, v26
	v_pk_add_f32 v[90:91], v[90:91], v[10:11]
	v_pk_add_f32 v[32:33], v[94:95], v[14:15]
	v_pk_mul_f32 v[90:91], v[90:91], v[26:27] op_sel_hi:[1,0]
	v_cvt_pk_fp8_f32 v95, v90, v91
	v_pk_mul_f32 v[32:33], v[32:33], v[26:27] op_sel_hi:[1,0]
	v_cvt_pk_fp8_f32 v94, v32, v33
	v_pk_add_f32 v[32:33], v[92:93], v[12:13]
	v_pk_add_f32 v[82:83], v[82:83], v[2:3]
	v_pk_mul_f32 v[32:33], v[32:33], v[26:27] op_sel_hi:[1,0]
	v_pk_mul_f32 v[82:83], v[82:83], v[26:27] op_sel_hi:[1,0]
	v_cvt_pk_fp8_f32 v95, v32, v33 op_sel:[0,0,1]
	v_pk_add_f32 v[32:33], v[86:87], v[6:7]
	v_pk_mul_f32 v[32:33], v[32:33], v[26:27] op_sel_hi:[1,0]
	v_pk_add_f32 v[30:31], v[96:97], v[16:17]
	v_cvt_pk_fp8_f32 v86, v32, v33
	v_cvt_pk_fp8_f32 v87, v82, v83
	v_pk_mul_f32 v[30:31], v[30:31], v[26:27] op_sel_hi:[1,0]
	v_pk_add_f32 v[32:33], v[84:85], v[4:5]
	v_cvt_pk_fp8_f32 v94, v30, v31 op_sel:[0,0,1]
	v_pk_add_f32 v[30:31], v[88:89], v[8:9]
	v_mov_b32_e32 v28, v167
	v_mov_b32_e32 v29, v24
	v_pk_mul_f32 v[30:31], v[30:31], v[26:27] op_sel_hi:[1,0]
	v_pk_mul_f32 v[32:33], v[32:33], v[26:27] op_sel_hi:[1,0]
	v_ashrrev_i64 v[28:29], 22, v[28:29]
	v_cvt_pk_fp8_f32 v86, v30, v31 op_sel:[0,0,1]
	v_cvt_pk_fp8_f32 v87, v32, v33 op_sel:[0,0,1]
	v_lshl_add_u64 v[28:29], s[2:3], 0, v[28:29]
	v_lshl_add_u64 v[28:29], v[28:29], 0, v[20:21]
	global_store_dwordx2 v[28:29], v[94:95], off
	global_store_dwordx2 v[28:29], v[86:87], off offset:128
.LBB0_886:
	s_or_b64 exec, exec, s[18:19]
	v_add_u32_e32 v24, 0x90, v162
	v_cmp_gt_i32_e32 vcc, s39, v24
	s_and_saveexec_b64 s[18:19], vcc
	s_cbranch_execz .LBB0_888
	v_mul_f32_e32 v26, 0x41800000, v27
	v_pk_add_f32 v[32:33], v[74:75], v[10:11]
	v_pk_mul_f32 v[32:33], v[32:33], v[26:27] op_sel_hi:[1,0]
	v_pk_add_f32 v[30:31], v[78:79], v[14:15]
	v_cvt_pk_fp8_f32 v75, v32, v33
	v_pk_mul_f32 v[30:31], v[30:31], v[26:27] op_sel_hi:[1,0]
	v_cvt_pk_fp8_f32 v74, v30, v31
	v_pk_add_f32 v[30:31], v[76:77], v[12:13]
	v_pk_add_f32 v[32:33], v[66:67], v[2:3]
	v_pk_mul_f32 v[30:31], v[30:31], v[26:27] op_sel_hi:[1,0]
	v_pk_mul_f32 v[32:33], v[32:33], v[26:27] op_sel_hi:[1,0]
	v_cvt_pk_fp8_f32 v75, v30, v31 op_sel:[0,0,1]
	v_pk_add_f32 v[30:31], v[70:71], v[6:7]
	v_pk_mul_f32 v[30:31], v[30:31], v[26:27] op_sel_hi:[1,0]
	v_pk_add_f32 v[28:29], v[80:81], v[16:17]
	v_cvt_pk_fp8_f32 v66, v30, v31
	v_cvt_pk_fp8_f32 v67, v32, v33
	v_pk_mul_f32 v[28:29], v[28:29], v[26:27] op_sel_hi:[1,0]
	v_pk_add_f32 v[30:31], v[68:69], v[4:5]
	v_cvt_pk_fp8_f32 v74, v28, v29 op_sel:[0,0,1]
	v_pk_add_f32 v[28:29], v[72:73], v[8:9]
	v_mov_b32_e32 v24, v167
	v_pk_mul_f32 v[28:29], v[28:29], v[26:27] op_sel_hi:[1,0]
	v_pk_mul_f32 v[26:27], v[30:31], v[26:27] op_sel_hi:[1,0]
	v_ashrrev_i64 v[24:25], 22, v[24:25]
	v_cvt_pk_fp8_f32 v66, v28, v29 op_sel:[0,0,1]
	v_cvt_pk_fp8_f32 v67, v26, v27 op_sel:[0,0,1]
	v_lshl_add_u64 v[24:25], s[2:3], 0, v[24:25]
	v_lshl_add_u64 v[24:25], v[24:25], 0, v[20:21]
	global_store_dwordx2 v[24:25], v[74:75], off
	global_store_dwordx2 v[24:25], v[66:67], off offset:128
.LBB0_888:
	s_or_b64 exec, exec, s[18:19]
	v_add_u32_e32 v24, 0xa0, v162
	v_cmp_gt_i32_e32 vcc, s39, v24
	s_and_saveexec_b64 s[18:19], vcc
	s_cbranch_execz .LBB0_890
	v_mul_f32_e32 v22, 0x41800000, v22
	v_pk_add_f32 v[30:31], v[58:59], v[10:11]
	v_pk_mul_f32 v[30:31], v[30:31], v[22:23] op_sel_hi:[1,0]
	v_pk_add_f32 v[28:29], v[62:63], v[14:15]
	v_cvt_pk_fp8_f32 v33, v30, v31
	v_pk_mul_f32 v[28:29], v[28:29], v[22:23] op_sel_hi:[1,0]
	v_cvt_pk_fp8_f32 v32, v28, v29
	v_pk_add_f32 v[28:29], v[60:61], v[12:13]
	v_pk_add_f32 v[30:31], v[50:51], v[2:3]
	v_pk_mul_f32 v[28:29], v[28:29], v[22:23] op_sel_hi:[1,0]
	v_pk_mul_f32 v[30:31], v[30:31], v[22:23] op_sel_hi:[1,0]
	v_cvt_pk_fp8_f32 v33, v28, v29 op_sel:[0,0,1]
	v_pk_add_f32 v[28:29], v[54:55], v[6:7]
	v_pk_mul_f32 v[28:29], v[28:29], v[22:23] op_sel_hi:[1,0]
	v_pk_add_f32 v[26:27], v[64:65], v[16:17]
	v_cvt_pk_fp8_f32 v50, v28, v29
	v_cvt_pk_fp8_f32 v51, v30, v31
	v_pk_mul_f32 v[26:27], v[26:27], v[22:23] op_sel_hi:[1,0]
	v_pk_add_f32 v[28:29], v[52:53], v[4:5]
	v_cvt_pk_fp8_f32 v32, v26, v27 op_sel:[0,0,1]
	v_pk_add_f32 v[26:27], v[56:57], v[8:9]
	v_mov_b32_e32 v24, v167
	v_mov_b32_e32 v25, v18
	v_pk_mul_f32 v[26:27], v[26:27], v[22:23] op_sel_hi:[1,0]
	v_pk_mul_f32 v[28:29], v[28:29], v[22:23] op_sel_hi:[1,0]
	v_ashrrev_i64 v[24:25], 22, v[24:25]
	v_cvt_pk_fp8_f32 v50, v26, v27 op_sel:[0,0,1]
	v_cvt_pk_fp8_f32 v51, v28, v29 op_sel:[0,0,1]
	v_lshl_add_u64 v[24:25], s[2:3], 0, v[24:25]
	v_lshl_add_u64 v[24:25], v[24:25], 0, v[20:21]
	global_store_dwordx2 v[24:25], v[32:33], off
	global_store_dwordx2 v[24:25], v[50:51], off offset:128
.LBB0_890:
	s_or_b64 exec, exec, s[18:19]
	v_add_u32_e32 v18, 0xb0, v162
	v_cmp_gt_i32_e32 vcc, s39, v18
	s_and_saveexec_b64 s[18:19], vcc
	s_cbranch_execz .LBB0_892
	v_mov_b32_e32 v18, v167
	v_ashrrev_i64 v[18:19], 22, v[18:19]
	v_mul_f32_e32 v22, 0x41800000, v23
	v_lshl_add_u64 v[18:19], s[2:3], 0, v[18:19]
	v_pk_add_f32 v[10:11], v[42:43], v[10:11]
	v_lshl_add_u64 v[18:19], v[18:19], 0, v[20:21]
	v_pk_add_f32 v[14:15], v[46:47], v[14:15]
	v_pk_mul_f32 v[10:11], v[10:11], v[22:23] op_sel_hi:[1,0]
	v_pk_add_f32 v[6:7], v[38:39], v[6:7]
	v_pk_add_f32 v[2:3], v[34:35], v[2:3]
	v_pk_mul_f32 v[14:15], v[14:15], v[22:23] op_sel_hi:[1,0]
	v_cvt_pk_fp8_f32 v21, v10, v11
	v_pk_mul_f32 v[6:7], v[6:7], v[22:23] op_sel_hi:[1,0]
	v_pk_mul_f32 v[2:3], v[2:3], v[22:23] op_sel_hi:[1,0]
	v_cvt_pk_fp8_f32 v20, v14, v15
	v_cvt_pk_fp8_f32 v10, v6, v7
	v_cvt_pk_fp8_f32 v11, v2, v3
	v_pk_add_f32 v[16:17], v[48:49], v[16:17]
	v_pk_add_f32 v[12:13], v[44:45], v[12:13]
	v_pk_add_f32 v[8:9], v[40:41], v[8:9]
	v_pk_add_f32 v[4:5], v[36:37], v[4:5]
	v_pk_mul_f32 v[16:17], v[16:17], v[22:23] op_sel_hi:[1,0]
	v_pk_mul_f32 v[12:13], v[12:13], v[22:23] op_sel_hi:[1,0]
	v_pk_mul_f32 v[8:9], v[8:9], v[22:23] op_sel_hi:[1,0]
	v_pk_mul_f32 v[4:5], v[4:5], v[22:23] op_sel_hi:[1,0]
	v_cvt_pk_fp8_f32 v20, v16, v17 op_sel:[0,0,1]
	v_cvt_pk_fp8_f32 v21, v12, v13 op_sel:[0,0,1]
	v_cvt_pk_fp8_f32 v10, v8, v9 op_sel:[0,0,1]
	v_cvt_pk_fp8_f32 v11, v4, v5 op_sel:[0,0,1]
	global_store_dwordx2 v[18:19], v[20:21], off
	global_store_dwordx2 v[18:19], v[10:11], off offset:128
